# speedup vs baseline: 1.0455x; 1.0152x over previous
.LBB0_5:
	v_add_u32_e32 v2, 0xffffff00, v0
	v_ashrrev_i32_e32 v2, 2, v2
	v_lshlrev_b32_e32 v1, 7, v1
	v_mad_i32_i24 v3, v2, s3, v1
	ds_read_b128 v[4:7], v3
	v_or_b32_e32 v8, 0x10c00, v1
	v_or_b32_e32 v12, 0x10e00, v1
	ds_read_b128 v[8:11], v8
	ds_read_b128 v[12:15], v12
	ds_read_b128 v[20:23], v3 offset:16
	ds_read_b128 v[24:27], v3 offset:32
	ds_read_b128 v[28:31], v3 offset:48
	s_waitcnt lgkmcnt(4)
	v_fma_f32 v16, v4, v8, 0
	s_waitcnt lgkmcnt(3)
	v_fma_f32 v17, v4, v12, 0
	v_or_b32_e32 v4, 0x10c10, v1
	v_fmac_f32_e32 v16, v5, v9
	v_fmac_f32_e32 v17, v5, v13
	v_or_b32_e32 v5, 0x10e10, v1
	ds_read_b128 v[32:35], v4
	ds_read_b128 v[36:39], v5
	v_fmac_f32_e32 v16, v6, v10
	v_fmac_f32_e32 v17, v6, v14
	v_fmac_f32_e32 v16, v7, v11
	v_or_b32_e32 v4, 0x10c20, v1
	v_or_b32_e32 v8, 0x10e20, v1
	v_fmac_f32_e32 v17, v7, v15
	s_waitcnt lgkmcnt(1)
	v_fmac_f32_e32 v16, v20, v32
	ds_read_b128 v[4:7], v4
	ds_read_b128 v[8:11], v8
	v_fmac_f32_e32 v16, v21, v33
	s_waitcnt lgkmcnt(2)
	v_fmac_f32_e32 v17, v20, v36
	v_fmac_f32_e32 v16, v22, v34
	v_fmac_f32_e32 v17, v21, v37
	v_fmac_f32_e32 v16, v23, v35
	v_fmac_f32_e32 v17, v22, v38
	s_waitcnt lgkmcnt(1)
	v_fmac_f32_e32 v16, v24, v4
	v_or_b32_e32 v4, 0x10c30, v1
	v_fmac_f32_e32 v17, v23, v39
	v_fmac_f32_e32 v16, v25, v5
	v_or_b32_e32 v5, 0x10e30, v1
	ds_read_b128 v[12:15], v4
	ds_read_b128 v[20:23], v5
	s_waitcnt lgkmcnt(2)
	v_fmac_f32_e32 v17, v24, v8
	v_fmac_f32_e32 v17, v25, v9
	v_fmac_f32_e32 v16, v26, v6
	v_fmac_f32_e32 v17, v26, v10
	v_fmac_f32_e32 v16, v27, v7
	v_or_b32_e32 v8, 0x10c40, v1
	v_fmac_f32_e32 v17, v27, v11
	s_waitcnt lgkmcnt(1)
	v_fmac_f32_e32 v16, v28, v12
	ds_read_b128 v[4:7], v3 offset:64
	v_or_b32_e32 v12, 0x10e40, v1
	ds_read_b128 v[8:11], v8
	ds_read_b128 v[24:27], v12
	s_waitcnt lgkmcnt(3)
	v_fmac_f32_e32 v17, v28, v20
	v_fmac_f32_e32 v16, v29, v13
	v_fmac_f32_e32 v17, v29, v21
	v_fmac_f32_e32 v16, v30, v14
	v_fmac_f32_e32 v17, v30, v22
	v_fmac_f32_e32 v16, v31, v15
	v_fmac_f32_e32 v17, v31, v23
	s_waitcnt lgkmcnt(1)
	v_fmac_f32_e32 v16, v4, v8
	s_waitcnt lgkmcnt(0)
	v_fmac_f32_e32 v17, v4, v24
	v_or_b32_e32 v4, 0x10c50, v1
	ds_read_b128 v[12:15], v3 offset:80
	v_fmac_f32_e32 v16, v5, v9
	v_fmac_f32_e32 v17, v5, v25
	v_or_b32_e32 v5, 0x10e50, v1
	ds_read_b128 v[20:23], v4
	ds_read_b128 v[28:31], v5
	v_fmac_f32_e32 v16, v6, v10
	v_fmac_f32_e32 v17, v6, v26
	v_fmac_f32_e32 v16, v7, v11
	v_fmac_f32_e32 v17, v7, v27
	v_or_b32_e32 v8, 0x10c60, v1
	s_waitcnt lgkmcnt(1)
	v_fmac_f32_e32 v16, v12, v20
	s_waitcnt lgkmcnt(0)
	v_fmac_f32_e32 v17, v12, v28
	ds_read_b128 v[4:7], v3 offset:96
	v_or_b32_e32 v12, 0x10e60, v1
	ds_read_b128 v[8:11], v8
	ds_read_b128 v[24:27], v12
	v_fmac_f32_e32 v16, v13, v21
	v_fmac_f32_e32 v17, v13, v29
	v_fmac_f32_e32 v16, v14, v22
	v_fmac_f32_e32 v17, v14, v30
	v_fmac_f32_e32 v16, v15, v23
	v_fmac_f32_e32 v17, v15, v31
	ds_read_b128 v[12:15], v3 offset:112
	v_or_b32_e32 v3, 0x10c70, v1
	v_or_b32_e32 v1, 0x10e70, v1
	ds_read_b128 v[20:23], v3
	ds_read_b128 v[28:31], v1
	s_waitcnt lgkmcnt(4)
	v_fmac_f32_e32 v16, v4, v8
	s_waitcnt lgkmcnt(3)
	v_fmac_f32_e32 v17, v4, v24
	v_fmac_f32_e32 v16, v5, v9
	v_fmac_f32_e32 v17, v5, v25
	v_fmac_f32_e32 v16, v6, v10
	v_fmac_f32_e32 v17, v6, v26
	v_fmac_f32_e32 v16, v7, v11
	v_fmac_f32_e32 v17, v7, v27
	s_waitcnt lgkmcnt(1)
	v_fmac_f32_e32 v16, v12, v20
	s_waitcnt lgkmcnt(0)
	v_fmac_f32_e32 v17, v12, v28
	v_fmac_f32_e32 v16, v13, v21
	v_fmac_f32_e32 v17, v13, v29
	v_fmac_f32_e32 v16, v14, v22
	v_fmac_f32_e32 v17, v14, v30
	v_fmac_f32_e32 v16, v15, v23
	v_fmac_f32_e32 v17, v15, v31
	ds_bpermute_b32 v1, v18, v16
	ds_bpermute_b32 v3, v18, v17
	s_waitcnt lgkmcnt(1)
	v_add_f32_e32 v1, v16, v1
	s_waitcnt lgkmcnt(0)
	v_add_f32_e32 v3, v17, v3
	ds_bpermute_b32 v4, v19, v1
	ds_bpermute_b32 v5, v19, v3
	s_and_saveexec_b64 s[4:5], vcc
	s_cbranch_execz .LBB0_7
	s_load_dwordx4 s[8:11], s[0:1], 0x20
	v_add_u32_e32 v2, s2, v2
	s_waitcnt lgkmcnt(0)
	v_add_f32_e32 v6, v3, v5
	v_ashrrev_i32_e32 v3, 31, v2
	v_add_f32_e32 v1, v1, v4
	v_lshlrev_b64 v[2:3], 2, v[2:3]
	v_mul_f32_e32 v1, 0x3fb8aa3b, v1
	v_lshl_add_u64 v[4:5], s[8:9], 0, v[2:3]
	global_store_dword v[4:5], v1, off sc0 sc1
	v_mul_f32_e32 v1, 0x3fb8aa3b, v6
	v_lshl_add_u64 v[2:3], s[10:11], 0, v[2:3]
	global_store_dword v[2:3], v1, off sc0 sc1

.LBB0_8:
	s_lshr_b32 s3, s6, 2
	v_bfe_u32 v32, v0, 5, 1
	v_and_b32_e32 v33, 31, v0
	s_and_b32 s3, s3, 32
	v_or_b32_e32 v0, s3, v33
	s_waitcnt lgkmcnt(1)
	v_lshlrev_b32_e32 v4, 4, v32
	s_movk_i32 s4, 0x110
	v_mad_u32_u24 v36, v0, s4, v4
	ds_read_b128 v[0:3], v36 offset:33792
	s_bfe_u32 s7, s6, 0x10006
	s_waitcnt lgkmcnt(1)
	v_lshl_or_b32 v5, s7, 5, v33
	v_mad_u32_u24 v34, v5, s4, v4
	ds_read_b128 v[4:7], v34 offset:51200
	ds_read_b128 v[16:19], v36 offset:33824
	ds_read_b128 v[20:23], v34 offset:51232
	s_waitcnt lgkmcnt(2)
	v_mfma_f32_32x32x16_f16 v[0:15], v[0:3], v[4:7], 0
	v_lshlrev_b32_e32 v42, 3, v32
	v_lshlrev_b32_e32 v40, 4, v33
	s_load_dwordx2 s[0:1], s[0:1], 0x18
	s_ashr_i32 s4, s2, 11
	s_and_b32 s2, s2, 0x7c0
	s_ashr_i32 s5, s4, 31
	s_lshr_b32 s6, s6, 6
	s_waitcnt lgkmcnt(0)
	v_mfma_f32_32x32x16_f16 v[0:15], v[16:19], v[20:23], v[0:15]
	ds_read_b128 v[16:19], v36 offset:33856
	ds_read_b128 v[20:23], v34 offset:51264
	ds_read_b128 v[24:27], v34 offset:51296
	ds_read_b128 v[28:31], v36 offset:33888
	s_or_b32 s8, s3, s2
	s_lshl_b64 s[2:3], s[4:5], 18
	s_add_u32 s2, s0, s2
	s_addc_u32 s3, s1, s3
	s_lshr_b32 s4, s8, 3
	s_or_b32 s0, s4, s7
	s_waitcnt lgkmcnt(2)
	v_mfma_f32_32x32x16_f16 v[0:15], v[16:19], v[20:23], v[0:15]
	ds_read_b128 v[16:19], v36 offset:33920
	ds_read_b128 v[20:23], v34 offset:51328
	s_lshl_b32 s0, s0, 10
	s_add_u32 s0, s2, s0
	v_mov_b32_e32 v41, 0
	s_addc_u32 s1, s3, 0
	s_or_b32 s4, s4, s6
	s_waitcnt lgkmcnt(2)
	v_mfma_f32_32x32x16_f16 v[0:15], v[28:31], v[24:27], v[0:15]
	ds_read_b128 v[24:27], v34 offset:51360
	ds_read_b128 v[28:31], v36 offset:33952
	v_mov_b32_e32 v43, v41
	s_waitcnt lgkmcnt(2)
	v_mfma_f32_32x32x16_f16 v[0:15], v[16:19], v[20:23], v[0:15]
	ds_read_b128 v[16:19], v34 offset:51392
	ds_read_b128 v[20:23], v34 offset:51424
	ds_read_b128 v[32:35], v36 offset:33984
	ds_read_b128 v[36:39], v36 offset:34016
	s_waitcnt lgkmcnt(4)
	v_mfma_f32_32x32x16_f16 v[0:15], v[28:31], v[24:27], v[0:15]
	v_lshl_add_u64 v[24:25], s[0:1], 0, v[40:41]
	s_lshl_b32 s0, s4, 10
	s_bitset1_b32 s0, 11
	s_add_u32 s0, s2, s0
	s_addc_u32 s1, s3, 0
	s_waitcnt lgkmcnt(1)
	v_mfma_f32_32x32x16_f16 v[0:15], v[32:35], v[16:19], v[0:15]
	v_lshl_add_u64 v[16:17], v[24:25], 0, v[42:43]
	v_lshl_add_u64 v[18:19], s[0:1], 0, v[40:41]
	v_lshl_add_u64 v[18:19], v[18:19], 0, v[42:43]
	s_waitcnt lgkmcnt(0)
	v_mfma_f32_32x32x16_f16 v[0:15], v[36:39], v[20:23], v[0:15]
	s_nop 11
	v_cvt_pk_f16_f32 v3, v2, v3
	v_cvt_pk_f16_f32 v2, v0, v1
	v_cvt_pk_f16_f32 v1, v6, v7
	v_cvt_pk_f16_f32 v0, v4, v5
	v_cvt_pk_f16_f32 v5, v10, v11
	v_cvt_pk_f16_f32 v4, v8, v9
	v_cvt_pk_f16_f32 v7, v14, v15
	v_cvt_pk_f16_f32 v6, v12, v13
	global_store_dwordx2 v[16:17], v[2:3], off sc0 sc1
	global_store_dwordx2 v[16:17], v[0:1], off offset:512 sc0 sc1
	global_store_dwordx2 v[18:19], v[4:5], off sc0 sc1
	global_store_dwordx2 v[18:19], v[6:7], off offset:512 sc0 sc1
	s_endpgm

.Lgm_no_fallback:
	v_lshrrev_b32_e32 v36, 5, v2
	v_lshlrev_b32_e32 v36, 10, v36
	v_and_b32_e32 v37, 31, v2
	v_lshl_add_u32 v36, v37, 2, v36
	v_div_scale_f32 v24, s[60:61], v48, v48, 1.0
	v_rcp_f32_e32 v25, v24
	s_nop 0
	v_fma_f32 v26, -v24, v25, 1.0
	v_fmac_f32_e32 v25, v26, v25
	v_div_scale_f32 v26, vcc, 1.0, v48, 1.0
	v_mul_f32_e32 v27, v26, v25
	v_fma_f32 v28, -v24, v27, v26
	v_fmac_f32_e32 v27, v28, v25
	v_fma_f32 v24, -v24, v27, v26
	s_nop 0
	v_div_fmas_f32 v24, v24, v25, v27
	v_div_fixup_f32 v25, v24, v48, 1.0
	v_mul_f32_e32 v29, v40, v25
	v_mul_f32_e32 v30, v44, v25
	v_cmp_eq_f32_e32 vcc, 0, v48
	s_nop 1
	v_cndmask_b32_e32 v29, v29, v88, vcc
	v_cndmask_b32_e32 v30, v30, v89, vcc
	v_mul_f32_e32 v24, 0x3fb8aa3b, v29
	v_mul_f32_e32 v26, 0x3fb8aa3b, v30
	v_exp_f32_e32 v24, v24
	v_exp_f32_e32 v26, v26
	s_nop 0
	v_add_f32_e32 v24, -1.0, v24
	v_add_f32_e32 v26, -1.0, v26
	v_cmp_lt_f32_e32 vcc, 0, v29
	s_nop 1
	v_cndmask_b32_e32 v24, v24, v29, vcc
	v_cmp_lt_f32_e32 vcc, 0, v30
	s_nop 1
	v_cndmask_b32_e32 v26, v26, v30, vcc
	global_store_dword v36, v24, s[12:13] sc0 sc1
	global_store_dword v36, v26, s[12:13] offset:128 sc0 sc1
	v_div_scale_f32 v24, s[60:61], v49, v49, 1.0
	v_rcp_f32_e32 v25, v24
	s_nop 0
	v_fma_f32 v26, -v24, v25, 1.0
	v_fmac_f32_e32 v25, v26, v25
	v_div_scale_f32 v26, vcc, 1.0, v49, 1.0
	v_mul_f32_e32 v27, v26, v25
	v_fma_f32 v28, -v24, v27, v26
	v_fmac_f32_e32 v27, v28, v25
	v_fma_f32 v24, -v24, v27, v26
	s_nop 0
	v_div_fmas_f32 v24, v24, v25, v27
	v_div_fixup_f32 v25, v24, v49, 1.0
	v_mul_f32_e32 v29, v41, v25
	v_mul_f32_e32 v30, v45, v25
	v_cmp_eq_f32_e32 vcc, 0, v49
	s_nop 1
	v_cndmask_b32_e32 v29, v29, v88, vcc
	v_cndmask_b32_e32 v30, v30, v89, vcc
	v_mul_f32_e32 v24, 0x3fb8aa3b, v29
	v_mul_f32_e32 v26, 0x3fb8aa3b, v30
	v_exp_f32_e32 v24, v24
	v_exp_f32_e32 v26, v26
	s_nop 0
	v_add_f32_e32 v24, -1.0, v24
	v_add_f32_e32 v26, -1.0, v26
	v_cmp_lt_f32_e32 vcc, 0, v29
	s_nop 1
	v_cndmask_b32_e32 v24, v24, v29, vcc
	v_cmp_lt_f32_e32 vcc, 0, v30
	s_nop 1
	v_cndmask_b32_e32 v26, v26, v30, vcc
	global_store_dword v36, v24, s[12:13] offset:256 sc0 sc1
	global_store_dword v36, v26, s[12:13] offset:384 sc0 sc1
	v_div_scale_f32 v24, s[60:61], v50, v50, 1.0
	v_rcp_f32_e32 v25, v24
	s_nop 0
	v_fma_f32 v26, -v24, v25, 1.0
	v_fmac_f32_e32 v25, v26, v25
	v_div_scale_f32 v26, vcc, 1.0, v50, 1.0
	v_mul_f32_e32 v27, v26, v25
	v_fma_f32 v28, -v24, v27, v26
	v_fmac_f32_e32 v27, v28, v25
	v_fma_f32 v24, -v24, v27, v26
	s_nop 0
	v_div_fmas_f32 v24, v24, v25, v27
	v_div_fixup_f32 v25, v24, v50, 1.0
	v_mul_f32_e32 v29, v42, v25
	v_mul_f32_e32 v30, v46, v25
	v_cmp_eq_f32_e32 vcc, 0, v50
	s_nop 1
	v_cndmask_b32_e32 v29, v29, v88, vcc
	v_cndmask_b32_e32 v30, v30, v89, vcc
	v_mul_f32_e32 v24, 0x3fb8aa3b, v29
	v_mul_f32_e32 v26, 0x3fb8aa3b, v30
	v_exp_f32_e32 v24, v24
	v_exp_f32_e32 v26, v26
	s_nop 0
	v_add_f32_e32 v24, -1.0, v24
	v_add_f32_e32 v26, -1.0, v26
	v_cmp_lt_f32_e32 vcc, 0, v29
	s_nop 1
	v_cndmask_b32_e32 v24, v24, v29, vcc
	v_cmp_lt_f32_e32 vcc, 0, v30
	s_nop 1
	v_cndmask_b32_e32 v26, v26, v30, vcc
	global_store_dword v36, v24, s[12:13] offset:512 sc0 sc1
	global_store_dword v36, v26, s[12:13] offset:640 sc0 sc1
	v_div_scale_f32 v24, s[60:61], v51, v51, 1.0
	v_rcp_f32_e32 v25, v24
	s_nop 0
	v_fma_f32 v26, -v24, v25, 1.0
	v_fmac_f32_e32 v25, v26, v25
	v_div_scale_f32 v26, vcc, 1.0, v51, 1.0
	v_mul_f32_e32 v27, v26, v25
	v_fma_f32 v28, -v24, v27, v26
	v_fmac_f32_e32 v27, v28, v25
	v_fma_f32 v24, -v24, v27, v26
	s_nop 0
	v_div_fmas_f32 v24, v24, v25, v27
	v_div_fixup_f32 v25, v24, v51, 1.0
	v_mul_f32_e32 v29, v43, v25
	v_mul_f32_e32 v30, v47, v25
	v_cmp_eq_f32_e32 vcc, 0, v51
	s_nop 1
	v_cndmask_b32_e32 v29, v29, v88, vcc
	v_cndmask_b32_e32 v30, v30, v89, vcc
	v_mul_f32_e32 v24, 0x3fb8aa3b, v29
	v_mul_f32_e32 v26, 0x3fb8aa3b, v30
	v_exp_f32_e32 v24, v24
	v_exp_f32_e32 v26, v26
	s_nop 0
	v_add_f32_e32 v24, -1.0, v24
	v_add_f32_e32 v26, -1.0, v26
	v_cmp_lt_f32_e32 vcc, 0, v29
	s_nop 1
	v_cndmask_b32_e32 v24, v24, v29, vcc
	v_cmp_lt_f32_e32 vcc, 0, v30
	s_nop 1
	v_cndmask_b32_e32 v26, v26, v30, vcc
	global_store_dword v36, v24, s[12:13] offset:768 sc0 sc1
	global_store_dword v36, v26, s[12:13] offset:896 sc0 sc1
	s_endpgm
